# c3 task-start waits counted (vmcnt(2): no longer wait for the previous task's two result stores), on top of mixer rewrite + flat release
# baseline (speedup 1.0000x reference)
.LBB0_658:
	v_writelane_b32 v247, s23, 38
	s_andn2_b64 vcc, exec, s[8:9]
	v_writelane_b32 v247, s91, 39
	s_cbranch_vccnz .LBB0_709
	v_readlane_b32 s0, v247, 36
	v_readlane_b32 s1, v247, 37
	s_lshl_b32 s66, s0, 7
	s_lshl_b64 s[0:1], s[66:67], 2
	s_add_u32 s0, s12, s0
	s_addc_u32 s1, s11, s1
	s_lshl_b32 s5, s4, 4
	s_cmp_gt_u32 s49, 1
	v_lshlrev_b32_e32 v36, 4, v35
	s_cselect_b64 s[94:95], -1, 0
	v_ashrrev_i32_e32 v104, 3, v35
	v_and_b32_e32 v36, 0x70, v36
	s_movk_i32 s11, 0x90
	s_and_b64 s[2:3], s[94:95], exec
	v_mad_u64_u32 v[90:91], s[2:3], v104, s11, v[36:37]
	s_cselect_b32 s64, 6, 0
	s_lshl_b32 s8, s4, 5
	v_lshlrev_b32_e32 v40, 3, v35
	s_ashr_i32 s2, s5, 31
	s_add_i32 s9, s8, 0
	v_lshl_add_u32 v37, v104, 1, 0
	v_and_b32_e32 v92, 0x78, v40
	v_and_b32_e32 v43, 15, v35
	v_mov_b32_e32 v41, s2
	s_ashr_i32 s2, s10, 3
	s_add_i32 s9, s9, 0x14800
	v_mul_u32_u24_e32 v39, 0x90, v36
	v_mad_u32_u24 v91, v36, s11, v37
	v_mov_b32_e32 v36, s5
	v_or_b32_e32 v40, s5, v43
	s_ashr_i32 s5, s4, 31
	s_and_b32 s3, s2, -16
	v_lshl_add_u32 v53, v43, 1, s9
	s_lshl_b32 s9, s4, 8
	s_add_i32 s35, 0, 0x14000
	v_lshlrev_b32_e32 v68, 2, v92
	s_lshl_b32 s34, s49, 6
	s_lshl_b32 s96, s49, 7
	v_bfi_b32 v42, -16, s2, v35
	s_add_i32 s2, s3, 64
	s_add_i32 s51, s35, s9
	v_lshl_add_u64 v[94:95], s[0:1], 0, v[68:69]
	s_lshl_b64 s[0:1], s[4:5], 10
	s_add_u32 s0, s38, s0
	v_lshlrev_b32_e32 v68, 4, v67
	s_addc_u32 s1, s39, s1
	s_movk_i32 s36, 0x48
	v_lshl_add_u64 v[44:45], s[0:1], 0, v[68:69]
	s_mov_b64 s[0:1], 0x5f17a100
	v_mul_f32_e32 v34, 0x4f7ffffe, v34
	v_lshrrev_b32_e32 v46, 4, v67
	v_mul_lo_u32 v47, v42, s36
	v_or_b32_e32 v42, s2, v43
	v_lshl_add_u64 v[96:97], v[44:45], 0, s[0:1]
	v_and_or_b32 v44, s8, 32, v43
	v_cvt_u32_f32_e32 v34, v34
	v_and_b32_e32 v38, 7, v35
	v_ashrrev_i32_e32 v106, 4, v35
	v_mul_lo_u32 v49, v42, s36
	v_lshl_or_b32 v51, v46, 2, s3
	v_and_b32_e32 v42, 48, v35
	v_mul_lo_u32 v35, v40, s11
	v_lshlrev_b64 v[40:41], 7, v[40:41]
	v_or_b32_e32 v79, 16, v44
	v_lshlrev_b32_e32 v48, 3, v46
	v_lshl_add_u64 v[40:41], s[6:7], 0, v[40:41]
	v_cmp_gt_i32_e64 s[4:5], v44, v51
	v_cmp_lt_i32_e64 s[6:7], v44, v51
	v_mul_lo_u32 v56, v51, s11
	v_or_b32_e32 v57, 1, v51
	v_or_b32_e32 v68, 2, v51
	v_or_b32_e32 v78, 3, v51
	v_cmp_gt_i32_e64 s[18:19], v79, v51
	v_cmp_lt_i32_e64 s[20:21], v79, v51
	v_lshlrev_b32_e32 v51, 1, v79
	v_mad_u32_u24 v105, v67, s11, v36
	v_or_b32_e32 v50, 0x1200, v48
	v_cmp_eq_u32_e64 s[2:3], 0, v43
	v_mul_u32_u24_e32 v45, 0x48, v44
	v_lshl_add_u32 v55, v44, 1, s92
	v_cmp_gt_i32_e64 s[8:9], v44, v57
	v_cmp_gt_i32_e64 s[10:11], v44, v68
	v_cmp_lt_i32_e64 s[12:13], v44, v68
	v_cmp_gt_i32_e64 s[14:15], v44, v78
	v_cmp_lt_i32_e64 s[16:17], v44, v78
	v_mad_u32_u24 v44, v44, s36, v240
	v_add3_u32 v108, s92, v56, v51
	v_cmp_gt_i32_e64 s[22:23], v79, v57
	v_cmp_gt_i32_e64 s[24:25], v79, v68
	v_cmp_lt_i32_e64 s[26:27], v79, v68
	v_mul_u32_u24_e32 v51, 0x48, v43
	v_mad_u32_u24 v57, v43, s36, v240
	v_mad_u32_u24 v68, v43, s36, v241
	v_mad_u32_u24 v43, v43, s36, v242
	s_movk_i32 s0, 0x88
	v_add_lshl_u32 v47, v47, v48, 1
	v_add_lshl_u32 v54, v45, v48, 1
	v_add_lshl_u32 v49, v49, v48, 1
	v_add_lshl_u32 v80, v44, v48, 1
	v_add_lshl_u32 v112, v48, v51, 1
	v_add_lshl_u32 v113, v57, v48, 1
	v_add_lshl_u32 v114, v68, v48, 1
	v_add_lshl_u32 v115, v43, v48, 1
	v_add_lshl_u32 v48, v50, v43, 1
	v_mul_lo_u32 v43, v106, s0
	s_sub_i32 s56, 0, s45
	v_readfirstlane_b32 s0, v34
	s_mul_i32 s1, s56, s0
	s_mul_hi_u32 s1, s0, s1
	s_add_i32 s57, s0, s1
	s_lshl_b32 s0, s49, 8
	s_add_u32 s0, s40, s0
	v_cmp_gt_i32_e64 s[28:29], v79, v78
	v_cmp_lt_i32_e64 s[30:31], v79, v78
	v_add_lshl_u32 v78, v50, v68, 1
	s_addc_u32 s1, s41, 0
	v_lshlrev_b32_e32 v68, 1, v92
	v_lshlrev_b32_e32 v36, 3, v38
	v_lshlrev_b32_e32 v38, 4, v38
	v_add_u32_e32 v52, 0, v42
	v_add_lshl_u32 v45, v45, v50, 1
	v_add_lshl_u32 v44, v44, v50, 1
	v_add_lshl_u32 v51, v50, v51, 1
	v_add_lshl_u32 v57, v50, v57, 1
	v_mul_u32_u24_e32 v46, 0x440, v46
	v_add_lshl_u32 v117, v43, v92, 1
	v_lshl_add_u64 v[98:99], s[0:1], 0, v[68:69]
	v_mov_b32_e32 v43, v69
	s_lshl_b32 s0, s45, 12
	v_add_u32_e32 v107, 32, v106
	v_lshl_add_u64 v[100:101], v[40:41], 0, v[42:43]
	s_lshl_b32 s36, s45, 6
	s_sub_i32 s37, 0, s0
	s_add_i32 s0, s84, s44
	v_add_u32_e32 v120, v37, v39
	v_lshlrev_b32_e32 v68, 1, v36
	v_lshlrev_b32_e32 v102, 1, v38
	v_add_u32_e32 v121, 0, v47
	v_add_u32_e32 v122, 0, v54
	v_add_u32_e32 v123, 0, v49
	v_add_u32_e32 v124, 0, v45
	v_add_u32_e32 v125, v55, v56
	v_add_u32_e32 v127, 0, v44
	v_add_u32_e32 v128, v52, v35
	v_add_u32_e32 v129, 0, v51
	v_add_u32_e32 v130, 0, v57
	v_add_u32_e32 v132, 0, v48
	v_add_u32_e32 v133, v53, v46
	s_waitcnt vmcnt(2)
	v_mov_b64_e32 v[54:55], v[62:63]
	v_mov_b64_e32 v[46:47], v[74:75]
	v_mov_b64_e32 v[50:51], v[58:59]
	v_mov_b64_e32 v[38:39], v[70:71]
	v_mov_b64_e32 v[44:45], v[20:21]
	v_mov_b64_e32 v[36:37], v[24:25]
	s_mov_b32 s97, s67
	v_mov_b32_e32 v93, v69
	v_add_u32_e32 v109, 0x90, v108
	v_add_u32_e32 v110, 0x120, v108
	v_add_u32_e32 v111, 0x1b0, v108
	v_lshl_add_u32 v116, v106, 2, s35
	v_lshl_add_u32 v118, v107, 2, s35
	v_add_u32_e32 v119, 0x2200, v117
	s_lshl_b32 s71, s44, 6
	s_lshl_b32 s74, s84, 6
	s_sub_i32 s75, 0, s36
	s_lshl_b32 s79, s44, 12
	s_lshl_b32 s80, s84, 12
	s_sub_i32 s81, 0xffffffc0, s0
	s_lshl_b32 s66, s34, 1
	v_add_u32_e32 v126, 0, v80
	v_add_u32_e32 v131, 0, v78
	v_mov_b64_e32 v[56:57], v[64:65]
	v_mov_b64_e32 v[48:49], v[76:77]
	v_mov_b64_e32 v[52:53], v[60:61]
	v_mov_b64_e32 v[40:41], v[72:73]
	v_mov_b64_e32 v[42:43], v[18:19]
	v_mov_b64_e32 v[34:35], v[22:23]
	s_waitcnt vmcnt(0)
	s_branch .LBB0_661

.LBB0_661:
	s_add_i32 s0, 0, 0x1b000
	v_add_u32_e32 v78, s0, v90
	v_readlane_b32 s34, v247, 23
	ds_write_b128 v78, v[14:17]
	v_mov_b32_e32 v86, v69
	v_add_u32_e32 v78, s34, v90
	ds_write_b128 v78, v[10:13]
	ds_write_b16 v120, v2 offset:54272
	ds_write_b16_d16_hi v120, v2 offset:54416
	ds_write_b16 v120, v3 offset:54560
	ds_write_b16_d16_hi v120, v3 offset:54704
	ds_write_b16 v120, v4 offset:54848
	ds_write_b16_d16_hi v120, v4 offset:54992
	ds_write_b16 v120, v5 offset:55136
	ds_write_b16_d16_hi v120, v5 offset:55280
	ds_write_b16 v91, v6 offset:55424
	ds_write_b16_d16_hi v91, v6 offset:55568
	ds_write_b16 v91, v7 offset:55712
	ds_write_b16_d16_hi v91, v7 offset:55856
	ds_write_b16 v91, v8 offset:56000
	ds_write_b16_d16_hi v91, v8 offset:56144
	ds_write_b16 v91, v9 offset:56288
	ds_write_b16_d16_hi v91, v9 offset:56432
	s_waitcnt vmcnt(2)
	v_lshlrev_b32_e32 v78, 16, v26
	v_and_b32_e32 v79, 0xffff0000, v26
	v_lshlrev_b32_e32 v80, 16, v27
	v_add_f32_dpp v78, v78, v78 row_shr:1 row_mask:0xf bank_mask:0xf bound_ctrl:1
	v_and_b32_e32 v81, 0xffff0000, v27
	v_lshlrev_b32_e32 v82, 16, v28
	v_add_f32_dpp v78, v78, v78 row_shr:2 row_mask:0xf bank_mask:0xf bound_ctrl:1
	v_and_b32_e32 v83, 0xffff0000, v28
	v_lshlrev_b32_e32 v84, 16, v29
	v_add_f32_dpp v78, v78, v78 row_shr:4 row_mask:0xf bank_mask:0xf bound_ctrl:1
	v_and_b32_e32 v85, 0xffff0000, v29
	v_mov_b32_e32 v87, v69
	v_add_f32_dpp v78, v78, v78 row_shr:8 row_mask:0xf bank_mask:0xf bound_ctrl:1
	s_waitcnt lgkmcnt(0)
	s_barrier
	s_add_i32 s65, s44, s84
	v_mov_b32_dpp v86, v78 row_bcast:15 row_mask:0xa bank_mask:0xf bound_ctrl:1
	v_add_f32_e32 v78, v78, v86
	v_mov_b32_e32 v86, v69
	s_add_i32 s85, s84, 64
	s_cmp_ge_i32 s85, s48
	v_mov_b32_dpp v86, v78 row_bcast:31 row_mask:0xc bank_mask:0xf bound_ctrl:1
	v_add_f32_e32 v103, v78, v86
	v_add_f32_dpp v78, v79, v79 row_shr:1 row_mask:0xf bank_mask:0xf bound_ctrl:1
	v_mov_b32_e32 v79, v69
	s_cselect_b64 s[86:87], -1, 0
	v_add_f32_dpp v78, v78, v78 row_shr:2 row_mask:0xf bank_mask:0xf bound_ctrl:1
	s_and_b64 vcc, exec, s[86:87]
	s_nop 0
	v_add_f32_dpp v78, v78, v78 row_shr:4 row_mask:0xf bank_mask:0xf bound_ctrl:1
	s_nop 1
	v_add_f32_dpp v78, v78, v78 row_shr:8 row_mask:0xf bank_mask:0xf bound_ctrl:1
	s_nop 1
	v_mov_b32_dpp v79, v78 row_bcast:15 row_mask:0xa bank_mask:0xf bound_ctrl:1
	v_add_f32_e32 v78, v78, v79
	v_mov_b32_e32 v79, v69
	s_nop 1
	v_mov_b32_dpp v79, v78 row_bcast:31 row_mask:0xc bank_mask:0xf bound_ctrl:1
	v_add_f32_e32 v146, v78, v79
	v_add_f32_dpp v78, v80, v80 row_shr:1 row_mask:0xf bank_mask:0xf bound_ctrl:1
	v_mov_b32_e32 v79, v69
	s_waitcnt vmcnt(2)
	v_lshlrev_b32_e32 v80, 16, v31
	v_add_f32_dpp v78, v78, v78 row_shr:2 row_mask:0xf bank_mask:0xf bound_ctrl:1
	s_nop 1
	v_add_f32_dpp v78, v78, v78 row_shr:4 row_mask:0xf bank_mask:0xf bound_ctrl:1
	s_nop 1
	v_add_f32_dpp v78, v78, v78 row_shr:8 row_mask:0xf bank_mask:0xf bound_ctrl:1
	s_nop 1
	v_mov_b32_dpp v79, v78 row_bcast:15 row_mask:0xa bank_mask:0xf bound_ctrl:1
	v_add_f32_e32 v78, v78, v79
	v_mov_b32_e32 v79, v69
	s_nop 1
	v_mov_b32_dpp v79, v78 row_bcast:31 row_mask:0xc bank_mask:0xf bound_ctrl:1
	v_add_f32_e32 v147, v78, v79
	v_add_f32_dpp v78, v81, v81 row_shr:1 row_mask:0xf bank_mask:0xf bound_ctrl:1
	v_mov_b32_e32 v79, v69
	v_and_b32_e32 v81, 0xffff0000, v31
	v_add_f32_dpp v78, v78, v78 row_shr:2 row_mask:0xf bank_mask:0xf bound_ctrl:1
	s_nop 1
	v_add_f32_dpp v78, v78, v78 row_shr:4 row_mask:0xf bank_mask:0xf bound_ctrl:1
	s_nop 1
	v_add_f32_dpp v78, v78, v78 row_shr:8 row_mask:0xf bank_mask:0xf bound_ctrl:1
	s_nop 1
	v_mov_b32_dpp v79, v78 row_bcast:15 row_mask:0xa bank_mask:0xf bound_ctrl:1
	v_add_f32_e32 v78, v78, v79
	v_mov_b32_e32 v79, v69
	s_nop 1
	v_mov_b32_dpp v79, v78 row_bcast:31 row_mask:0xc bank_mask:0xf bound_ctrl:1
	v_add_f32_e32 v148, v78, v79
	v_add_f32_dpp v78, v82, v82 row_shr:1 row_mask:0xf bank_mask:0xf bound_ctrl:1
	v_mov_b32_e32 v79, v69
	v_lshlrev_b32_e32 v82, 16, v32
	v_add_f32_dpp v78, v78, v78 row_shr:2 row_mask:0xf bank_mask:0xf bound_ctrl:1
	s_nop 1
	v_add_f32_dpp v78, v78, v78 row_shr:4 row_mask:0xf bank_mask:0xf bound_ctrl:1
	s_nop 1
	v_add_f32_dpp v78, v78, v78 row_shr:8 row_mask:0xf bank_mask:0xf bound_ctrl:1
	s_nop 1
	v_mov_b32_dpp v79, v78 row_bcast:15 row_mask:0xa bank_mask:0xf bound_ctrl:1
	v_add_f32_e32 v78, v78, v79
	v_mov_b32_e32 v79, v69
	s_nop 1
	v_mov_b32_dpp v79, v78 row_bcast:31 row_mask:0xc bank_mask:0xf bound_ctrl:1
	v_add_f32_e32 v149, v78, v79
	v_add_f32_dpp v78, v83, v83 row_shr:1 row_mask:0xf bank_mask:0xf bound_ctrl:1
	v_mov_b32_e32 v79, v69
	v_and_b32_e32 v83, 0xffff0000, v32
	v_add_f32_dpp v78, v78, v78 row_shr:2 row_mask:0xf bank_mask:0xf bound_ctrl:1
	s_nop 1
	v_add_f32_dpp v78, v78, v78 row_shr:4 row_mask:0xf bank_mask:0xf bound_ctrl:1
	s_nop 1
	v_add_f32_dpp v78, v78, v78 row_shr:8 row_mask:0xf bank_mask:0xf bound_ctrl:1
	s_nop 1
	v_mov_b32_dpp v79, v78 row_bcast:15 row_mask:0xa bank_mask:0xf bound_ctrl:1
	v_add_f32_e32 v78, v78, v79
	v_mov_b32_e32 v79, v69
	s_nop 1
	v_mov_b32_dpp v79, v78 row_bcast:31 row_mask:0xc bank_mask:0xf bound_ctrl:1
	v_add_f32_e32 v150, v78, v79
	v_add_f32_dpp v78, v84, v84 row_shr:1 row_mask:0xf bank_mask:0xf bound_ctrl:1
	v_mov_b32_e32 v79, v69
	v_lshlrev_b32_e32 v84, 16, v33
	v_add_f32_dpp v78, v78, v78 row_shr:2 row_mask:0xf bank_mask:0xf bound_ctrl:1
	s_nop 1
	v_add_f32_dpp v78, v78, v78 row_shr:4 row_mask:0xf bank_mask:0xf bound_ctrl:1
	s_nop 1
	v_add_f32_dpp v78, v78, v78 row_shr:8 row_mask:0xf bank_mask:0xf bound_ctrl:1
	s_nop 1
	v_mov_b32_dpp v79, v78 row_bcast:15 row_mask:0xa bank_mask:0xf bound_ctrl:1
	v_add_f32_e32 v78, v78, v79
	v_mov_b32_e32 v79, v69
	s_nop 1
	v_mov_b32_dpp v79, v78 row_bcast:31 row_mask:0xc bank_mask:0xf bound_ctrl:1
	v_add_f32_e32 v151, v78, v79
	v_add_f32_dpp v78, v85, v85 row_shr:1 row_mask:0xf bank_mask:0xf bound_ctrl:1
	v_mov_b32_e32 v79, v69
	v_and_b32_e32 v85, 0xffff0000, v33
	v_add_f32_dpp v78, v78, v78 row_shr:2 row_mask:0xf bank_mask:0xf bound_ctrl:1
	s_nop 1
	v_add_f32_dpp v78, v78, v78 row_shr:4 row_mask:0xf bank_mask:0xf bound_ctrl:1
	s_nop 1
	v_add_f32_dpp v78, v78, v78 row_shr:8 row_mask:0xf bank_mask:0xf bound_ctrl:1
	s_nop 1
	v_mov_b32_dpp v79, v78 row_bcast:15 row_mask:0xa bank_mask:0xf bound_ctrl:1
	v_add_f32_e32 v78, v78, v79
	v_mov_b32_e32 v79, v69
	s_nop 1
	v_mov_b32_dpp v79, v78 row_bcast:31 row_mask:0xc bank_mask:0xf bound_ctrl:1
	v_add_f32_e32 v152, v78, v79
	v_lshlrev_b32_e32 v78, 16, v30
	v_and_b32_e32 v79, 0xffff0000, v30
	s_nop 0
	v_add_f32_dpp v86, v78, v78 row_shr:1 row_mask:0xf bank_mask:0xf bound_ctrl:1
	s_nop 1
	v_add_f32_dpp v86, v86, v86 row_shr:2 row_mask:0xf bank_mask:0xf bound_ctrl:1
	s_nop 1
	v_add_f32_dpp v86, v86, v86 row_shr:4 row_mask:0xf bank_mask:0xf bound_ctrl:1
	s_nop 1
	v_add_f32_dpp v86, v86, v86 row_shr:8 row_mask:0xf bank_mask:0xf bound_ctrl:1
	s_nop 1
	v_mov_b32_dpp v87, v86 row_bcast:15 row_mask:0xa bank_mask:0xf bound_ctrl:1
	v_add_f32_e32 v86, v86, v87
	v_mov_b32_e32 v87, v69
	s_nop 1
	v_mov_b32_dpp v87, v86 row_bcast:31 row_mask:0xc bank_mask:0xf bound_ctrl:1
	v_add_f32_e32 v86, v86, v87
	v_mul_f32_e32 v87, 0x3fb8aa3b, v146
	v_readlane_b32 s1, v86, 63
	v_exp_f32_e32 v87, v87
	s_nop 0
	v_sub_f32_e32 v86, s1, v86
	v_add_f32_e32 v153, v86, v78
	v_add_f32_dpp v78, v79, v79 row_shr:1 row_mask:0xf bank_mask:0xf bound_ctrl:1
	v_mov_b32_e32 v86, v69
	s_nop 0
	v_add_f32_dpp v78, v78, v78 row_shr:2 row_mask:0xf bank_mask:0xf bound_ctrl:1
	s_nop 1
	v_add_f32_dpp v78, v78, v78 row_shr:4 row_mask:0xf bank_mask:0xf bound_ctrl:1
	s_nop 1
	v_add_f32_dpp v78, v78, v78 row_shr:8 row_mask:0xf bank_mask:0xf bound_ctrl:1
	s_nop 1
	v_mov_b32_dpp v86, v78 row_bcast:15 row_mask:0xa bank_mask:0xf bound_ctrl:1
	v_add_f32_e32 v78, v78, v86
	v_mov_b32_e32 v86, v69
	s_nop 1
	v_mov_b32_dpp v86, v78 row_bcast:31 row_mask:0xc bank_mask:0xf bound_ctrl:1
	v_add_f32_e32 v78, v78, v86
	v_mul_f32_e32 v86, 0x3fb8aa3b, v103
	v_readlane_b32 s1, v78, 63
	v_exp_f32_e32 v86, v86
	s_nop 0
	v_sub_f32_e32 v78, s1, v78
	v_add_f32_e32 v154, v78, v79
	v_mov_b32_e32 v79, v69
	v_add_f32_dpp v78, v80, v80 row_shr:1 row_mask:0xf bank_mask:0xf bound_ctrl:1
	s_nop 1
	v_add_f32_dpp v78, v78, v78 row_shr:2 row_mask:0xf bank_mask:0xf bound_ctrl:1
	s_nop 1
	v_add_f32_dpp v78, v78, v78 row_shr:4 row_mask:0xf bank_mask:0xf bound_ctrl:1
	s_nop 1
	v_add_f32_dpp v78, v78, v78 row_shr:8 row_mask:0xf bank_mask:0xf bound_ctrl:1
	s_nop 1
	v_mov_b32_dpp v79, v78 row_bcast:15 row_mask:0xa bank_mask:0xf bound_ctrl:1
	v_add_f32_e32 v78, v78, v79
	v_mov_b32_e32 v79, v69
	s_nop 1
	v_mov_b32_dpp v79, v78 row_bcast:31 row_mask:0xc bank_mask:0xf bound_ctrl:1
	v_add_f32_e32 v78, v78, v79
	v_mov_b32_e32 v79, v69
	v_readlane_b32 s1, v78, 63
	s_nop 1
	v_sub_f32_e32 v78, s1, v78
	v_add_f32_e32 v155, v78, v80
	s_nop 0
	v_add_f32_dpp v78, v81, v81 row_shr:1 row_mask:0xf bank_mask:0xf bound_ctrl:1
	s_nop 1
	v_add_f32_dpp v78, v78, v78 row_shr:2 row_mask:0xf bank_mask:0xf bound_ctrl:1
	s_nop 1
	v_add_f32_dpp v78, v78, v78 row_shr:4 row_mask:0xf bank_mask:0xf bound_ctrl:1
	s_nop 1
	v_add_f32_dpp v78, v78, v78 row_shr:8 row_mask:0xf bank_mask:0xf bound_ctrl:1
	s_nop 1
	v_mov_b32_dpp v79, v78 row_bcast:15 row_mask:0xa bank_mask:0xf bound_ctrl:1
	v_add_f32_e32 v78, v78, v79
	v_mov_b32_e32 v79, v69
	s_nop 1
	v_mov_b32_dpp v79, v78 row_bcast:31 row_mask:0xc bank_mask:0xf bound_ctrl:1
	v_add_f32_e32 v78, v78, v79
	v_mov_b32_e32 v79, v69
	v_readlane_b32 s1, v78, 63
	s_nop 1
	v_sub_f32_e32 v78, s1, v78
	v_add_f32_e32 v156, v78, v81
	s_nop 0
	v_add_f32_dpp v78, v82, v82 row_shr:1 row_mask:0xf bank_mask:0xf bound_ctrl:1
	s_nop 1
	v_add_f32_dpp v78, v78, v78 row_shr:2 row_mask:0xf bank_mask:0xf bound_ctrl:1
	s_nop 1
	v_add_f32_dpp v78, v78, v78 row_shr:4 row_mask:0xf bank_mask:0xf bound_ctrl:1
	s_nop 1
	v_add_f32_dpp v78, v78, v78 row_shr:8 row_mask:0xf bank_mask:0xf bound_ctrl:1
	s_nop 1
	v_mov_b32_dpp v79, v78 row_bcast:15 row_mask:0xa bank_mask:0xf bound_ctrl:1
	v_add_f32_e32 v78, v78, v79
	v_mov_b32_e32 v79, v69
	s_nop 1
	v_mov_b32_dpp v79, v78 row_bcast:31 row_mask:0xc bank_mask:0xf bound_ctrl:1
	v_add_f32_e32 v78, v78, v79
	v_mov_b32_e32 v79, v69
	v_readlane_b32 s1, v78, 63
	s_nop 1
	v_sub_f32_e32 v78, s1, v78
	v_add_f32_e32 v157, v78, v82
	v_add_u32_e32 v82, s0, v105
	v_add_f32_dpp v78, v83, v83 row_shr:1 row_mask:0xf bank_mask:0xf bound_ctrl:1
	s_mov_b32 s0, 0x3e000000
	s_nop 0
	v_add_f32_dpp v78, v78, v78 row_shr:2 row_mask:0xf bank_mask:0xf bound_ctrl:1
	s_nop 1
	v_add_f32_dpp v78, v78, v78 row_shr:4 row_mask:0xf bank_mask:0xf bound_ctrl:1
	s_nop 1
	v_add_f32_dpp v78, v78, v78 row_shr:8 row_mask:0xf bank_mask:0xf bound_ctrl:1
	s_nop 1
	v_mov_b32_dpp v79, v78 row_bcast:15 row_mask:0xa bank_mask:0xf bound_ctrl:1
	v_add_f32_e32 v78, v78, v79
	v_mov_b32_e32 v79, v69
	s_nop 1
	v_mov_b32_dpp v79, v78 row_bcast:31 row_mask:0xc bank_mask:0xf bound_ctrl:1
	v_add_f32_e32 v78, v78, v79
	v_mov_b32_e32 v79, v69
	v_readlane_b32 s1, v78, 63
	s_nop 1
	v_sub_f32_e32 v78, s1, v78
	v_add_f32_e32 v158, v78, v83
	s_nop 0
	v_add_f32_dpp v78, v84, v84 row_shr:1 row_mask:0xf bank_mask:0xf bound_ctrl:1
	s_nop 1
	v_add_f32_dpp v78, v78, v78 row_shr:2 row_mask:0xf bank_mask:0xf bound_ctrl:1
	s_nop 1
	v_add_f32_dpp v78, v78, v78 row_shr:4 row_mask:0xf bank_mask:0xf bound_ctrl:1
	s_nop 1
	v_add_f32_dpp v78, v78, v78 row_shr:8 row_mask:0xf bank_mask:0xf bound_ctrl:1
	s_nop 1
	v_mov_b32_dpp v79, v78 row_bcast:15 row_mask:0xa bank_mask:0xf bound_ctrl:1
	v_add_f32_e32 v78, v78, v79
	v_mov_b32_e32 v79, v69
	s_nop 1
	v_mov_b32_dpp v79, v78 row_bcast:31 row_mask:0xc bank_mask:0xf bound_ctrl:1
	v_add_f32_e32 v78, v78, v79
	v_mov_b32_e32 v79, v69
	v_readlane_b32 s1, v78, 63
	s_nop 1
	v_sub_f32_e32 v78, s1, v78
	v_add_f32_e32 v159, v78, v84
	s_nop 0
	v_add_f32_dpp v78, v85, v85 row_shr:1 row_mask:0xf bank_mask:0xf bound_ctrl:1
	s_nop 1
	v_add_f32_dpp v78, v78, v78 row_shr:2 row_mask:0xf bank_mask:0xf bound_ctrl:1
	s_nop 1
	v_add_f32_dpp v78, v78, v78 row_shr:4 row_mask:0xf bank_mask:0xf bound_ctrl:1
	s_nop 1
	v_add_f32_dpp v78, v78, v78 row_shr:8 row_mask:0xf bank_mask:0xf bound_ctrl:1
	s_nop 1
	v_mov_b32_dpp v79, v78 row_bcast:15 row_mask:0xa bank_mask:0xf bound_ctrl:1
	v_add_f32_e32 v78, v78, v79
	v_mov_b32_e32 v79, v69
	s_nop 1
	v_mov_b32_dpp v79, v78 row_bcast:31 row_mask:0xc bank_mask:0xf bound_ctrl:1
	v_add_f32_e32 v78, v78, v79
	s_nop 0
	v_readlane_b32 s1, v78, 63
	s_nop 1
	v_sub_f32_e32 v78, s1, v78
	v_add_f32_e32 v160, v78, v85
	v_add_u32_e32 v78, s34, v105
	ds_read_b128 v[78:81], v78
	ds_read_b128 v[82:85], v82
	s_waitcnt lgkmcnt(1)
	v_lshlrev_b32_e32 v88, 16, v78
	v_and_b32_e32 v89, 0xffff0000, v78
	v_mul_f32_e32 v78, 0x3fb8aa3b, v147
	v_exp_f32_e32 v134, v78
	v_mul_f32_e32 v78, 0x3fb8aa3b, v148
	v_exp_f32_e32 v135, v78
	v_lshlrev_b32_e32 v78, 16, v79
	v_and_b32_e32 v79, 0xffff0000, v79
	v_pk_mul_f32 v[136:137], v[78:79], s[0:1] op_sel_hi:[1,0]
	v_mul_f32_e32 v78, 0x3fb8aa3b, v149
	v_mul_f32_e32 v79, 0x3fb8aa3b, v150
	v_exp_f32_e32 v78, v78
	v_exp_f32_e32 v79, v79
	v_lshlrev_b32_e32 v138, 16, v80
	v_and_b32_e32 v139, 0xffff0000, v80
	v_pk_mul_f32 v[138:139], v[138:139], s[0:1] op_sel_hi:[1,0]
	v_lshlrev_b32_e32 v80, 16, v81
	v_pk_mul_f32 v[140:141], v[78:79], v[138:139]
	v_mul_f32_e32 v78, 0x3fb8aa3b, v151
	v_mul_f32_e32 v79, 0x3fb8aa3b, v152
	v_exp_f32_e32 v78, v78
	v_exp_f32_e32 v79, v79
	v_and_b32_e32 v81, 0xffff0000, v81
	v_pk_mul_f32 v[88:89], v[88:89], s[0:1] op_sel_hi:[1,0]
	v_pk_mul_f32 v[142:143], v[80:81], s[0:1] op_sel_hi:[1,0]
	v_pk_mul_f32 v[86:87], v[86:87], v[88:89]
	v_pk_mul_f32 v[134:135], v[134:135], v[136:137]
	v_pk_mul_f32 v[144:145], v[78:79], v[142:143]
	v_cvt_pk_bf16_f32 v78, v86, v87
	v_cvt_pk_bf16_f32 v79, v134, v135
	v_cvt_pk_bf16_f32 v80, v140, v141
	v_cvt_pk_bf16_f32 v81, v144, v145
	v_add_u32_e32 v140, 0, v105
	ds_write_b128 v140, v[78:81] offset:35840
	v_mul_f32_e32 v78, 0x3fb8aa3b, v153
	v_mul_f32_e32 v79, 0x3fb8aa3b, v154
	v_exp_f32_e32 v78, v78
	v_exp_f32_e32 v79, v79
	v_mul_f32_e32 v80, 0x3fb8aa3b, v155
	v_mul_f32_e32 v81, 0x3fb8aa3b, v156
	v_mul_f32_e32 v86, 0x3fb8aa3b, v157
	v_pk_mul_f32 v[78:79], v[78:79], v[88:89]
	v_mul_f32_e32 v87, 0x3fb8aa3b, v158
	v_mul_f32_e32 v88, 0x3fb8aa3b, v159
	v_mul_f32_e32 v89, 0x3fb8aa3b, v160
	v_exp_f32_e32 v80, v80
	v_exp_f32_e32 v81, v81
	v_exp_f32_e32 v86, v86
	v_exp_f32_e32 v87, v87
	v_exp_f32_e32 v88, v88
	v_exp_f32_e32 v89, v89
	v_pk_mul_f32 v[80:81], v[80:81], v[136:137]
	v_pk_mul_f32 v[86:87], v[86:87], v[138:139]
	v_cvt_pk_bf16_f32 v78, v78, v79
	v_pk_mul_f32 v[88:89], v[88:89], v[142:143]
	v_cvt_pk_bf16_f32 v79, v80, v81
	v_cvt_pk_bf16_f32 v80, v86, v87
	v_cvt_pk_bf16_f32 v81, v88, v89
	s_waitcnt lgkmcnt(1)
	v_lshlrev_b32_e32 v134, 16, v84
	v_and_b32_e32 v135, 0xffff0000, v84
	v_mul_f32_e32 v84, 0xbfb8aa3b, v151
	ds_write_b128 v140, v[78:81] offset:45056
	v_mul_f32_e32 v78, 0xbfb8aa3b, v103
	v_mul_f32_e32 v79, 0xbfb8aa3b, v146
	v_mul_f32_e32 v80, 0xbfb8aa3b, v147
	v_mul_f32_e32 v81, 0xbfb8aa3b, v148
	v_mul_f32_e32 v88, 0xbfb8aa3b, v149
	v_mul_f32_e32 v89, 0xbfb8aa3b, v150
	v_exp_f32_e32 v136, v84
	v_mul_f32_e32 v84, 0xbfb8aa3b, v152
	v_exp_f32_e32 v78, v78
	v_exp_f32_e32 v79, v79
	v_exp_f32_e32 v80, v80
	v_exp_f32_e32 v81, v81
	v_exp_f32_e32 v88, v88
	v_exp_f32_e32 v89, v89
	v_exp_f32_e32 v137, v84
	v_lshlrev_b32_e32 v86, 16, v82
	v_and_b32_e32 v87, 0xffff0000, v82
	v_lshlrev_b32_e32 v82, 16, v83
	v_and_b32_e32 v83, 0xffff0000, v83
	v_lshlrev_b32_e32 v84, 16, v85
	v_and_b32_e32 v85, 0xffff0000, v85
	v_pk_mul_f32 v[78:79], v[78:79], v[86:87]
	v_pk_mul_f32 v[80:81], v[80:81], v[82:83]
	v_pk_mul_f32 v[88:89], v[88:89], v[134:135]
	v_pk_mul_f32 v[136:137], v[136:137], v[84:85]
	v_cvt_pk_bf16_f32 v78, v78, v79
	v_cvt_pk_bf16_f32 v79, v80, v81
	v_cvt_pk_bf16_f32 v80, v88, v89
	v_cvt_pk_bf16_f32 v81, v136, v137
	ds_write_b128 v140, v[78:81] offset:17408
	v_mul_f32_e32 v78, 0xbfb8aa3b, v153
	v_mul_f32_e32 v79, 0xbfb8aa3b, v154
	v_mul_f32_e32 v80, 0xbfb8aa3b, v155
	v_mul_f32_e32 v81, 0xbfb8aa3b, v156
	v_exp_f32_e32 v78, v78
	v_exp_f32_e32 v79, v79
	v_exp_f32_e32 v80, v80
	v_exp_f32_e32 v81, v81
	v_pk_mul_f32 v[78:79], v[78:79], v[86:87]
	v_mul_f32_e32 v86, 0xbfb8aa3b, v159
	v_pk_mul_f32 v[80:81], v[80:81], v[82:83]
	v_mul_f32_e32 v82, 0xbfb8aa3b, v157
	v_mul_f32_e32 v83, 0xbfb8aa3b, v158
	v_mul_f32_e32 v87, 0xbfb8aa3b, v160
	v_exp_f32_e32 v82, v82
	v_exp_f32_e32 v83, v83
	v_exp_f32_e32 v86, v86
	v_exp_f32_e32 v87, v87
	v_cvt_pk_bf16_f32 v78, v78, v79
	v_pk_mul_f32 v[82:83], v[82:83], v[134:135]
	v_cvt_pk_bf16_f32 v79, v80, v81
	v_pk_mul_f32 v[84:85], v[86:87], v[84:85]
	v_cvt_pk_bf16_f32 v80, v82, v83
	v_cvt_pk_bf16_f32 v81, v84, v85
	ds_write_b128 v140, v[78:81] offset:26624
	s_cbranch_vccnz .LBB0_676
	s_ashr_i32 s89, s85, 31
	s_add_i32 s0, s84, s89
	s_add_i32 s0, s0, 64
	s_xor_b32 s0, s0, s89
	s_mul_hi_u32 s1, s0, s57
	s_mul_i32 s34, s1, s45
	s_sub_i32 s0, s0, s34
	s_add_i32 s34, s1, 1
	s_sub_i32 s35, s0, s45
	s_cmp_ge_u32 s0, s45
	s_cselect_b32 s1, s34, s1
	s_cselect_b32 s0, s35, s0
	s_add_i32 s34, s1, 1
	s_cmp_ge_u32 s0, s45
	s_cselect_b32 s0, s34, s1
	s_xor_b32 s90, s0, s89
	s_sub_i32 s88, s90, s89
	s_mul_i32 s0, s56, s88
	s_add_i32 s91, s65, s0
	s_add_i32 s69, s91, 64
	s_cmp_lt_i32 s69, 4
	s_mov_b64 s[34:35], -1
	s_cselect_b64 s[0:1], -1, 0
	s_cmp_gt_i32 s69, 3
	s_mul_i32 s70, s36, s88
	s_cbranch_scc1 .LBB0_664
	s_lshl_b32 s34, s90, 8
	s_sub_i32 s34, s34, s70
	s_lshl_b32 s35, s89, 8
	s_sub_i32 s34, s34, s35
	s_add_i32 s35, s71, s74
	s_add_i32 s34, s35, s34
	s_add_i32 s77, s34, 0x1000
	s_mov_b64 s[34:35], 0
